# unchanged conversion kernel; gather by LDS-DMA in wide-load layout, 40 KB static LDS (4 workgroups per CU)
# baseline (speedup 1.0000x reference)
_Z10cvt_kernelPKDv4_fPDv4_DF16_:
	s_load_dwordx4 s[4:7], s[0:1], 0x0
	s_and_b32 s0, s2, 7
	s_mulk_i32 s0, 0xf42
	s_lshr_b32 s1, s2, 3
	s_add_i32 s0, s0, s1
	s_cmpk_lt_u32 s2, 0x7a10
	s_cselect_b32 s0, s0, s2
	s_ashr_i32 s1, s0, 31
	s_lshl_b64 s[0:1], s[0:1], 9
	v_or_b32_e32 v8, s0, v0
	v_mov_b32_e32 v9, s1
	s_waitcnt lgkmcnt(0)
	v_lshl_add_u64 v[4:5], v[8:9], 4, s[4:5]
	s_movk_i32 s0, 0x1000
	global_load_dwordx4 v[0:3], v[4:5], off nt
	v_add_co_u32_e32 v4, vcc, s0, v4
	v_lshl_add_u64 v[8:9], v[8:9], 3, s[6:7]
	s_nop 0
	v_addc_co_u32_e32 v5, vcc, 0, v5, vcc
	global_load_dwordx4 v[4:7], v[4:5], off nt
	s_waitcnt vmcnt(1)
	v_cvt_pk_f16_f32 v3, v2, v3
	v_cvt_pk_f16_f32 v2, v0, v1
	s_waitcnt vmcnt(0)
	v_cvt_pk_f16_f32 v1, v6, v7
	v_cvt_pk_f16_f32 v0, v4, v5
	global_store_dwordx2 v[8:9], v[2:3], off sc1
	global_store_dwordx2 v[8:9], v[0:1], off offset:2048 sc1
	s_endpgm

	.amdhsa_kernel _Z10cvt_kernelPKDv4_fPDv4_DF16_
		.amdhsa_group_segment_fixed_size 0
		.amdhsa_private_segment_fixed_size 0
		.amdhsa_kernarg_size 16
		.amdhsa_user_sgpr_count 2
		.amdhsa_user_sgpr_dispatch_ptr 0
		.amdhsa_user_sgpr_queue_ptr 0
		.amdhsa_user_sgpr_kernarg_segment_ptr 1
		.amdhsa_user_sgpr_dispatch_id 0
		.amdhsa_user_sgpr_kernarg_preload_length 0
		.amdhsa_user_sgpr_kernarg_preload_offset 0
		.amdhsa_user_sgpr_private_segment_size 0
		.amdhsa_uses_dynamic_stack 0
		.amdhsa_enable_private_segment 0
		.amdhsa_system_sgpr_workgroup_id_x 1
		.amdhsa_system_sgpr_workgroup_id_y 0
		.amdhsa_system_sgpr_workgroup_id_z 0
		.amdhsa_system_sgpr_workgroup_info 0
		.amdhsa_system_vgpr_workitem_id 0
		.amdhsa_next_free_vgpr 10
		.amdhsa_next_free_sgpr 8
		.amdhsa_accum_offset 12
		.amdhsa_reserve_vcc 1
		.amdhsa_float_round_mode_32 0
		.amdhsa_float_round_mode_16_64 0
		.amdhsa_float_denorm_mode_32 3
		.amdhsa_float_denorm_mode_16_64 3
		.amdhsa_dx10_clamp 1
		.amdhsa_ieee_mode 1
		.amdhsa_fp16_overflow 0
		.amdhsa_tg_split 0
		.amdhsa_exception_fp_ieee_invalid_op 0
		.amdhsa_exception_fp_denorm_src 0
		.amdhsa_exception_fp_ieee_div_zero 0
		.amdhsa_exception_fp_ieee_overflow 0
		.amdhsa_exception_fp_ieee_underflow 0
		.amdhsa_exception_fp_ieee_inexact 0
		.amdhsa_exception_int_div_zero 0
	.end_amdhsa_kernel

amdhsa.kernels:
  - .agpr_count:     0
    .args:
      - .actual_access:  read_only
        .address_space:  global
        .offset:         0
        .size:           8
        .value_kind:     global_buffer
      - .actual_access:  write_only
        .address_space:  global
        .offset:         8
        .size:           8
        .value_kind:     global_buffer
    .group_segment_fixed_size: 0
    .kernarg_segment_align: 8
    .kernarg_segment_size: 16
    .language:       OpenCL C
    .language_version:
      - 2
      - 0
    .max_flat_workgroup_size: 256
    .name:           _Z10cvt_kernelPKDv4_fPDv4_DF16_
    .private_segment_fixed_size: 0
    .sgpr_count:     14
    .sgpr_spill_count: 0
    .symbol:         _Z10cvt_kernelPKDv4_fPDv4_DF16_.kd
    .uniform_work_group_size: 1
    .uses_dynamic_stack: false
    .vgpr_count:     10
    .vgpr_spill_count: 0
    .wavefront_size: 64
  - .agpr_count:     0
    .args:
      - .actual_access:  read_only
        .address_space:  global
        .offset:         0
        .size:           8
        .value_kind:     global_buffer
      - .actual_access:  read_only
        .address_space:  global
        .offset:         8
        .size:           8
        .value_kind:     global_buffer
      - .actual_access:  write_only
        .address_space:  global
        .offset:         16
        .size:           8
        .value_kind:     global_buffer
    .group_segment_fixed_size: 40960
    .kernarg_segment_align: 8
    .kernarg_segment_size: 24
    .language:       OpenCL C
    .language_version:
      - 2
      - 0
    .max_flat_workgroup_size: 256
    .name:           _Z13gather_kernelPKDv2_DF16_PKiPf
    .private_segment_fixed_size: 0
    .sgpr_count:     22
    .sgpr_spill_count: 0
    .symbol:         _Z13gather_kernelPKDv2_DF16_PKiPf.kd
    .uniform_work_group_size: 1
    .uses_dynamic_stack: false
    .vgpr_count:     64
    .vgpr_spill_count: 0
    .wavefront_size: 64
